# v010 + MoE-down leftover panels: split-K small tile 64x32 -> 64x64 (A fragments shared by twice the MFMAs, a third less L2 traffic), reduction + store once per 32-column half
# speedup vs baseline: 1.0110x; 1.0110x over previous
; template <int NS  > __device__ __forceinline__ f32x4 ctx_tile(Frame& F, const bf16* A, const bf16* Bt, int r0, int c0) {
;     ...
;     const bf16* ap = A + (size_t)(r0 + l15) * K + w * (K / 8) + 8 * g;
;     const bf16* bp = Bt + (size_t)(c0 + l15) * K + w * (K / 8) + 8 * g;
;     f32x4 acc[4][2];
; #pragma unroll
;     for (int rt = 0; rt < 4; ++rt) { acc[rt][0] = (f32x4){0.f, 0.f, 0.f, 0.f}; acc[rt][1] = (f32x4){0.f, 0.f, 0.f, 0.f}; }
; #pragma unroll 4
;     for (int s = 0; s < NS; ++s) {
;         bf16x8 af[4], bf[2];
; #pragma unroll
;         for (int rt = 0; rt < 4; ++rt) af[rt] = *(const bf16x8*)(ap + (size_t)(16 * rt) * K + 32 * s);
;         bf[0] = *(const bf16x8*)(bp + 32 * s); bf[1] = *(const bf16x8*)(bp + (size_t)16 * K + 32 * s);
; #pragma unroll
;         for (int rt = 0; rt < 4; ++rt) { acc[rt][0] = __builtin_amdgcn_mfma_f32_16x16x32_bf16(bf[0], af[rt], acc[rt][0], 0, 0, 0); acc[rt][1] = __builtin_amdgcn_mfma_f32_16x16x32_bf16(bf[1], af[rt], acc[rt][1], 0, 0, 0); }
; __global__ void __launch_bounds__(NWAVES * 64, 2) mk_fwd(Args args) {
;     ...
;                 for (int tl = F.vcu; tl < (np - npm) * 128; tl += F.G) {
;                     const int pm = npm + (tl >> 7), r0 = 256 * pm + 64 * ((tl >> 5) & 3), c0 = 32 * (tl & 31);
;                     const int e = __builtin_amdgcn_readfirstlane(((const int*)(ws + WS_PANELE))[pm]);
;                     const f32x4 s = ctx_tile<14>(F, (const bf16*)(ws + WS_HID), (const bf16*)(ws + WS_EXP + (l >> 1) * EXP_STRIDE) + (size_t)NE * 2 * DFE * D + (size_t)e * D * DFE, r0, c0);
.LBB13_1580:
	s_lshl_b32 s10, s41, 6
	s_cmp_ge_i32 s29, s10
	s_cbranch_scc1 .LBB13_1583
	s_mul_i32 s8, s30, 0x1c0
	s_ashr_i32 s9, s8, 31
	v_lshrrev_b32_e32 v2, 1, v1
	s_lshl_b64 s[4:5], s[8:9], 1
	v_and_b32_e32 v2, 24, v2
	s_add_u32 s4, s37, s4
	s_addc_u32 s5, s38, s5
	v_lshlrev_b32_e32 v4, 1, v2
	v_mov_b32_e32 v5, v98
	v_lshl_add_u64 v[58:59], s[4:5], 0, v[4:5]
	s_lshl_b32 s4, s30, 13
	v_and_b32_e32 v4, 0xfffffc0, v1
	v_lshlrev_b32_e32 v3, 4, v99
	s_add_i32 s4, s31, s4
	v_lshlrev_b32_e32 v4, 4, v4
	v_add_u32_e32 v63, s4, v3
	v_add3_u32 v64, s31, v3, v4
	v_ashrrev_i32_e32 v3, 3, v1
	v_and_b32_e32 v62, 15, v1
	v_bfi_b32 v65, -16, v3, v1
	v_lshrrev_b32_e32 v1, 2, v1
	v_and_b32_e32 v1, 28, v1
	s_lshl_b32 s11, s29, 1
	s_lshl_b32 s12, s28, 1
	s_lshl_b32 s13, s29, 5
	s_lshl_b32 s14, s28, 5
	v_lshlrev_b32_e32 v60, 1, v2
.LBB13_1582:
	s_ashr_i32 s4, s29, 6
	s_add_i32 s4, s4, s36
	s_lshl_b32 s6, s29, 6
	s_and_b32 s6, s6, 0xc0
	s_lshl_b32 s15, s29, 4
	s_and_b32 s15, s15, 0x3c0
	s_lshl_b32 s7, s4, 8
	s_ashr_i32 s5, s4, 31
	v_or_b32_e32 v2, s15, v62
	s_or_b32 s16, s7, s6
	s_lshl_b64 s[4:5], s[4:5], 2
	v_mul_u32_u24_e32 v2, 0xe00, v2
	s_add_u32 s4, s2, s4
	v_lshlrev_b32_e32 v10, 1, v2
	v_or_b32_e32 v2, s16, v62
	s_addc_u32 s5, s3, s5
	v_mad_i64_i32 v[30:31], s[6:7], v2, s86, v[58:59]
	global_load_dword v12, v98, s[4:5]
	s_mov_b32 s4, 0x38000
	v_add_co_u32_e32 v32, vcc, s90, v30
	v_add_co_u32_e64 v50, s[4:5], s4, v30
	s_nop 0
	v_addc_co_u32_e32 v33, vcc, 0, v31, vcc
	v_addc_co_u32_e64 v51, vcc, 0, v31, s[4:5]
	v_mov_b32_e32 v11, v98
	s_mov_b32 s6, 0x54000
	v_mov_b32_e32 v61, v98
	v_add_co_u32_e64 v54, s[6:7], s6, v30
	s_nop 1
	v_addc_co_u32_e64 v55, vcc, 0, v31, s[6:7]
	global_load_dwordx4 v[68:71], v[30:31], off
	global_load_dwordx4 v[72:75], v[32:33], off
	global_load_dwordx4 v[76:79], v[50:51], off
	global_load_dwordx4 v[80:83], v[54:55], off
	global_load_dwordx4 v[84:87], v[30:31], off offset:64
	global_load_dwordx4 v[88:91], v[32:33], off offset:64
	global_load_dwordx4 v[92:95], v[50:51], off offset:64
	global_load_dwordx4 v[100:103], v[54:55], off offset:64
	global_load_dwordx4 v[104:107], v[30:31], off offset:128
	global_load_dwordx4 v[108:111], v[32:33], off offset:128
	global_load_dwordx4 v[112:115], v[50:51], off offset:128
	global_load_dwordx4 v[116:119], v[54:55], off offset:128
	s_waitcnt vmcnt(12)
	v_readfirstlane_b32 s4, v12
	s_mul_hi_i32 s5, s4, 0x700000
	s_mul_i32 s4, s4, 0x700000
	s_add_u32 s4, s34, s4
	s_addc_u32 s5, s35, s5
	v_lshl_add_u64 v[10:11], s[4:5], 0, v[10:11]
	v_lshl_add_u64 v[10:11], s[8:9], 1, v[10:11]
	v_lshl_add_u64 v[52:53], v[10:11], 0, v[60:61]
	v_add_co_u32_e32 v56, vcc, s90, v52
	s_nop 1
	v_addc_co_u32_e32 v57, vcc, 0, v53, vcc
	v_add_co_u32_e32 v208, vcc, s90, v56
	s_nop 1
	v_addc_co_u32_e32 v209, vcc, 0, v57, vcc
	v_add_co_u32_e32 v210, vcc, s90, v208
	s_nop 1
	v_addc_co_u32_e32 v211, vcc, 0, v209, vcc
	global_load_dwordx4 v[120:123], v[52:53], off
	global_load_dwordx4 v[124:127], v[56:57], off
	global_load_dwordx4 v[128:131], v[208:209], off
	global_load_dwordx4 v[132:135], v[210:211], off
	global_load_dwordx4 v[136:139], v[52:53], off offset:64
	global_load_dwordx4 v[140:143], v[56:57], off offset:64
	global_load_dwordx4 v[144:147], v[208:209], off offset:64
	global_load_dwordx4 v[148:151], v[210:211], off offset:64
	global_load_dwordx4 v[152:155], v[52:53], off offset:128
	global_load_dwordx4 v[156:159], v[56:57], off offset:128
	global_load_dwordx4 v[160:163], v[208:209], off offset:128
	global_load_dwordx4 v[164:167], v[210:211], off offset:128
	s_waitcnt vmcnt(8)
	v_mfma_f32_16x16x32_bf16 v[4:7], v[120:123], v[68:71], 0
	v_mfma_f32_16x16x32_bf16 v[8:11], v[124:127], v[68:71], 0
	v_mfma_f32_16x16x32_bf16 v[180:183], v[128:131], v[68:71], 0
	v_mfma_f32_16x16x32_bf16 v[184:187], v[132:135], v[68:71], 0
	v_mfma_f32_16x16x32_bf16 v[12:15], v[120:123], v[72:75], 0
	v_mfma_f32_16x16x32_bf16 v[16:19], v[124:127], v[72:75], 0
	v_mfma_f32_16x16x32_bf16 v[188:191], v[128:131], v[72:75], 0
	v_mfma_f32_16x16x32_bf16 v[192:195], v[132:135], v[72:75], 0
	v_mfma_f32_16x16x32_bf16 v[20:23], v[120:123], v[76:79], 0
	v_mfma_f32_16x16x32_bf16 v[24:27], v[124:127], v[76:79], 0
	v_mfma_f32_16x16x32_bf16 v[212:215], v[128:131], v[76:79], 0
	v_mfma_f32_16x16x32_bf16 v[216:219], v[132:135], v[76:79], 0
	v_mfma_f32_16x16x32_bf16 v[44:47], v[120:123], v[80:83], 0
	v_mfma_f32_16x16x32_bf16 v[244:247], v[124:127], v[80:83], 0
	v_mfma_f32_16x16x32_bf16 v[220:223], v[128:131], v[80:83], 0
	v_mfma_f32_16x16x32_bf16 v[224:227], v[132:135], v[80:83], 0
	global_load_dwordx4 v[168:171], v[30:31], off offset:192
	global_load_dwordx4 v[172:175], v[32:33], off offset:192
	global_load_dwordx4 v[176:179], v[50:51], off offset:192
	global_load_dwordx4 v[228:231], v[54:55], off offset:192
	global_load_dwordx4 v[68:71], v[52:53], off offset:192
	global_load_dwordx4 v[72:75], v[56:57], off offset:192
	global_load_dwordx4 v[76:79], v[208:209], off offset:192
	global_load_dwordx4 v[80:83], v[210:211], off offset:192
	s_waitcnt vmcnt(12)
; template <int NS  > __device__ __forceinline__ f32x4 ctx_tile(Frame& F, const bf16* A, const bf16* Bt, int r0, int c0) {
;     ...
;     for (int s = 0; s < NS; ++s) {
;         bf16x8 af[4], bf[2];
; #pragma unroll
;         for (int rt = 0; rt < 4; ++rt) af[rt] = *(const bf16x8*)(ap + (size_t)(16 * rt) * K + 32 * s);
;         bf[0] = *(const bf16x8*)(bp + 32 * s); bf[1] = *(const bf16x8*)(bp + (size_t)16 * K + 32 * s);
; #pragma unroll
;         for (int rt = 0; rt < 4; ++rt) { acc[rt][0] = __builtin_amdgcn_mfma_f32_16x16x32_bf16(bf[0], af[rt], acc[rt][0], 0, 0, 0); acc[rt][1] = __builtin_amdgcn_mfma_f32_16x16x32_bf16(bf[1], af[rt], acc[rt][1], 0, 0, 0); }
;     }
	v_mfma_f32_16x16x32_bf16 v[4:7], v[136:139], v[84:87], v[4:7]
	v_mfma_f32_16x16x32_bf16 v[8:11], v[140:143], v[84:87], v[8:11]
	v_mfma_f32_16x16x32_bf16 v[180:183], v[144:147], v[84:87], v[180:183]
	v_mfma_f32_16x16x32_bf16 v[184:187], v[148:151], v[84:87], v[184:187]
	v_mfma_f32_16x16x32_bf16 v[12:15], v[136:139], v[88:91], v[12:15]
	v_mfma_f32_16x16x32_bf16 v[16:19], v[140:143], v[88:91], v[16:19]
	v_mfma_f32_16x16x32_bf16 v[188:191], v[144:147], v[88:91], v[188:191]
	v_mfma_f32_16x16x32_bf16 v[192:195], v[148:151], v[88:91], v[192:195]
	v_mfma_f32_16x16x32_bf16 v[20:23], v[136:139], v[92:95], v[20:23]
	v_mfma_f32_16x16x32_bf16 v[24:27], v[140:143], v[92:95], v[24:27]
	v_mfma_f32_16x16x32_bf16 v[212:215], v[144:147], v[92:95], v[212:215]
	v_mfma_f32_16x16x32_bf16 v[216:219], v[148:151], v[92:95], v[216:219]
	v_mfma_f32_16x16x32_bf16 v[44:47], v[136:139], v[100:103], v[44:47]
	v_mfma_f32_16x16x32_bf16 v[244:247], v[140:143], v[100:103], v[244:247]
	v_mfma_f32_16x16x32_bf16 v[220:223], v[144:147], v[100:103], v[220:223]
	v_mfma_f32_16x16x32_bf16 v[224:227], v[148:151], v[100:103], v[224:227]
	global_load_dwordx4 v[120:123], v[30:31], off offset:256
	global_load_dwordx4 v[124:127], v[32:33], off offset:256
	global_load_dwordx4 v[128:131], v[50:51], off offset:256
	global_load_dwordx4 v[132:135], v[54:55], off offset:256
	global_load_dwordx4 v[84:87], v[52:53], off offset:256
	global_load_dwordx4 v[88:91], v[56:57], off offset:256
	global_load_dwordx4 v[92:95], v[208:209], off offset:256
	global_load_dwordx4 v[100:103], v[210:211], off offset:256
	s_waitcnt vmcnt(16)
	v_mfma_f32_16x16x32_bf16 v[4:7], v[152:155], v[104:107], v[4:7]
	v_mfma_f32_16x16x32_bf16 v[8:11], v[156:159], v[104:107], v[8:11]
	v_mfma_f32_16x16x32_bf16 v[180:183], v[160:163], v[104:107], v[180:183]
	v_mfma_f32_16x16x32_bf16 v[184:187], v[164:167], v[104:107], v[184:187]
	v_mfma_f32_16x16x32_bf16 v[12:15], v[152:155], v[108:111], v[12:15]
	v_mfma_f32_16x16x32_bf16 v[16:19], v[156:159], v[108:111], v[16:19]
	v_mfma_f32_16x16x32_bf16 v[188:191], v[160:163], v[108:111], v[188:191]
	v_mfma_f32_16x16x32_bf16 v[192:195], v[164:167], v[108:111], v[192:195]
	v_mfma_f32_16x16x32_bf16 v[20:23], v[152:155], v[112:115], v[20:23]
	v_mfma_f32_16x16x32_bf16 v[24:27], v[156:159], v[112:115], v[24:27]
	v_mfma_f32_16x16x32_bf16 v[212:215], v[160:163], v[112:115], v[212:215]
	v_mfma_f32_16x16x32_bf16 v[216:219], v[164:167], v[112:115], v[216:219]
	v_mfma_f32_16x16x32_bf16 v[44:47], v[152:155], v[116:119], v[44:47]
	v_mfma_f32_16x16x32_bf16 v[244:247], v[156:159], v[116:119], v[244:247]
	v_mfma_f32_16x16x32_bf16 v[220:223], v[160:163], v[116:119], v[220:223]
	v_mfma_f32_16x16x32_bf16 v[224:227], v[164:167], v[116:119], v[224:227]
	global_load_dwordx4 v[136:139], v[30:31], off offset:320
	global_load_dwordx4 v[140:143], v[32:33], off offset:320
	global_load_dwordx4 v[144:147], v[50:51], off offset:320
	global_load_dwordx4 v[148:151], v[54:55], off offset:320
	global_load_dwordx4 v[104:107], v[52:53], off offset:320
	global_load_dwordx4 v[108:111], v[56:57], off offset:320
	global_load_dwordx4 v[112:115], v[208:209], off offset:320
	global_load_dwordx4 v[116:119], v[210:211], off offset:320
	s_waitcnt vmcnt(16)
	v_mfma_f32_16x16x32_bf16 v[4:7], v[68:71], v[168:171], v[4:7]
	v_mfma_f32_16x16x32_bf16 v[8:11], v[72:75], v[168:171], v[8:11]
	v_mfma_f32_16x16x32_bf16 v[180:183], v[76:79], v[168:171], v[180:183]
	v_mfma_f32_16x16x32_bf16 v[184:187], v[80:83], v[168:171], v[184:187]
	v_mfma_f32_16x16x32_bf16 v[12:15], v[68:71], v[172:175], v[12:15]
	v_mfma_f32_16x16x32_bf16 v[16:19], v[72:75], v[172:175], v[16:19]
	v_mfma_f32_16x16x32_bf16 v[188:191], v[76:79], v[172:175], v[188:191]
	v_mfma_f32_16x16x32_bf16 v[192:195], v[80:83], v[172:175], v[192:195]
	v_mfma_f32_16x16x32_bf16 v[20:23], v[68:71], v[176:179], v[20:23]
	v_mfma_f32_16x16x32_bf16 v[24:27], v[72:75], v[176:179], v[24:27]
	v_mfma_f32_16x16x32_bf16 v[212:215], v[76:79], v[176:179], v[212:215]
	v_mfma_f32_16x16x32_bf16 v[216:219], v[80:83], v[176:179], v[216:219]
	v_mfma_f32_16x16x32_bf16 v[44:47], v[68:71], v[228:231], v[44:47]
	v_mfma_f32_16x16x32_bf16 v[244:247], v[72:75], v[228:231], v[244:247]
	v_mfma_f32_16x16x32_bf16 v[220:223], v[76:79], v[228:231], v[220:223]
	v_mfma_f32_16x16x32_bf16 v[224:227], v[80:83], v[228:231], v[224:227]
	global_load_dwordx4 v[152:155], v[30:31], off offset:384
	global_load_dwordx4 v[156:159], v[32:33], off offset:384
	global_load_dwordx4 v[160:163], v[50:51], off offset:384
	global_load_dwordx4 v[164:167], v[54:55], off offset:384
	global_load_dwordx4 v[168:171], v[52:53], off offset:384
	global_load_dwordx4 v[172:175], v[56:57], off offset:384
	global_load_dwordx4 v[176:179], v[208:209], off offset:384
	global_load_dwordx4 v[228:231], v[210:211], off offset:384
	s_waitcnt vmcnt(16)
	v_mfma_f32_16x16x32_bf16 v[4:7], v[84:87], v[120:123], v[4:7]
	v_mfma_f32_16x16x32_bf16 v[8:11], v[88:91], v[120:123], v[8:11]
	v_mfma_f32_16x16x32_bf16 v[180:183], v[92:95], v[120:123], v[180:183]
	v_mfma_f32_16x16x32_bf16 v[184:187], v[100:103], v[120:123], v[184:187]
	v_mfma_f32_16x16x32_bf16 v[12:15], v[84:87], v[124:127], v[12:15]
	v_mfma_f32_16x16x32_bf16 v[16:19], v[88:91], v[124:127], v[16:19]
	v_mfma_f32_16x16x32_bf16 v[188:191], v[92:95], v[124:127], v[188:191]
	v_mfma_f32_16x16x32_bf16 v[192:195], v[100:103], v[124:127], v[192:195]
	v_mfma_f32_16x16x32_bf16 v[20:23], v[84:87], v[128:131], v[20:23]
	v_mfma_f32_16x16x32_bf16 v[24:27], v[88:91], v[128:131], v[24:27]
	v_mfma_f32_16x16x32_bf16 v[212:215], v[92:95], v[128:131], v[212:215]
	v_mfma_f32_16x16x32_bf16 v[216:219], v[100:103], v[128:131], v[216:219]
	v_mfma_f32_16x16x32_bf16 v[44:47], v[84:87], v[132:135], v[44:47]
	v_mfma_f32_16x16x32_bf16 v[244:247], v[88:91], v[132:135], v[244:247]
	v_mfma_f32_16x16x32_bf16 v[220:223], v[92:95], v[132:135], v[220:223]
	v_mfma_f32_16x16x32_bf16 v[224:227], v[100:103], v[132:135], v[224:227]
	global_load_dwordx4 v[68:71], v[30:31], off offset:448
	global_load_dwordx4 v[72:75], v[32:33], off offset:448
	global_load_dwordx4 v[76:79], v[50:51], off offset:448
	global_load_dwordx4 v[80:83], v[54:55], off offset:448
	global_load_dwordx4 v[120:123], v[52:53], off offset:448
	global_load_dwordx4 v[124:127], v[56:57], off offset:448
	global_load_dwordx4 v[128:131], v[208:209], off offset:448
	global_load_dwordx4 v[132:135], v[210:211], off offset:448
	s_waitcnt vmcnt(16)
; template <int NS  > __device__ __forceinline__ f32x4 ctx_tile(Frame& F, const bf16* A, const bf16* Bt, int r0, int c0) {
;     ...
;     for (int s = 0; s < NS; ++s) {
;         bf16x8 af[4], bf[2];
; #pragma unroll
;         for (int rt = 0; rt < 4; ++rt) af[rt] = *(const bf16x8*)(ap + (size_t)(16 * rt) * K + 32 * s);
;         bf[0] = *(const bf16x8*)(bp + 32 * s); bf[1] = *(const bf16x8*)(bp + (size_t)16 * K + 32 * s);
; #pragma unroll
;         for (int rt = 0; rt < 4; ++rt) { acc[rt][0] = __builtin_amdgcn_mfma_f32_16x16x32_bf16(bf[0], af[rt], acc[rt][0], 0, 0, 0); acc[rt][1] = __builtin_amdgcn_mfma_f32_16x16x32_bf16(bf[1], af[rt], acc[rt][1], 0, 0, 0); }
;     }
	v_mfma_f32_16x16x32_bf16 v[4:7], v[104:107], v[136:139], v[4:7]
	v_mfma_f32_16x16x32_bf16 v[8:11], v[108:111], v[136:139], v[8:11]
	v_mfma_f32_16x16x32_bf16 v[180:183], v[112:115], v[136:139], v[180:183]
	v_mfma_f32_16x16x32_bf16 v[184:187], v[116:119], v[136:139], v[184:187]
	v_mfma_f32_16x16x32_bf16 v[12:15], v[104:107], v[140:143], v[12:15]
	v_mfma_f32_16x16x32_bf16 v[16:19], v[108:111], v[140:143], v[16:19]
	v_mfma_f32_16x16x32_bf16 v[188:191], v[112:115], v[140:143], v[188:191]
	v_mfma_f32_16x16x32_bf16 v[192:195], v[116:119], v[140:143], v[192:195]
	v_mfma_f32_16x16x32_bf16 v[20:23], v[104:107], v[144:147], v[20:23]
	v_mfma_f32_16x16x32_bf16 v[24:27], v[108:111], v[144:147], v[24:27]
	v_mfma_f32_16x16x32_bf16 v[212:215], v[112:115], v[144:147], v[212:215]
	v_mfma_f32_16x16x32_bf16 v[216:219], v[116:119], v[144:147], v[216:219]
	v_mfma_f32_16x16x32_bf16 v[44:47], v[104:107], v[148:151], v[44:47]
	v_mfma_f32_16x16x32_bf16 v[244:247], v[108:111], v[148:151], v[244:247]
	v_mfma_f32_16x16x32_bf16 v[220:223], v[112:115], v[148:151], v[220:223]
	v_mfma_f32_16x16x32_bf16 v[224:227], v[116:119], v[148:151], v[224:227]
	global_load_dwordx4 v[84:87], v[30:31], off offset:512
	global_load_dwordx4 v[88:91], v[32:33], off offset:512
	global_load_dwordx4 v[92:95], v[50:51], off offset:512
	global_load_dwordx4 v[100:103], v[54:55], off offset:512
	global_load_dwordx4 v[136:139], v[52:53], off offset:512
	global_load_dwordx4 v[140:143], v[56:57], off offset:512
	global_load_dwordx4 v[144:147], v[208:209], off offset:512
	global_load_dwordx4 v[148:151], v[210:211], off offset:512
	s_waitcnt vmcnt(16)
	v_mfma_f32_16x16x32_bf16 v[4:7], v[168:171], v[152:155], v[4:7]
	v_mfma_f32_16x16x32_bf16 v[8:11], v[172:175], v[152:155], v[8:11]
	v_mfma_f32_16x16x32_bf16 v[180:183], v[176:179], v[152:155], v[180:183]
	v_mfma_f32_16x16x32_bf16 v[184:187], v[228:231], v[152:155], v[184:187]
	v_mfma_f32_16x16x32_bf16 v[12:15], v[168:171], v[156:159], v[12:15]
	v_mfma_f32_16x16x32_bf16 v[16:19], v[172:175], v[156:159], v[16:19]
	v_mfma_f32_16x16x32_bf16 v[188:191], v[176:179], v[156:159], v[188:191]
	v_mfma_f32_16x16x32_bf16 v[192:195], v[228:231], v[156:159], v[192:195]
	v_mfma_f32_16x16x32_bf16 v[20:23], v[168:171], v[160:163], v[20:23]
	v_mfma_f32_16x16x32_bf16 v[24:27], v[172:175], v[160:163], v[24:27]
	v_mfma_f32_16x16x32_bf16 v[212:215], v[176:179], v[160:163], v[212:215]
	v_mfma_f32_16x16x32_bf16 v[216:219], v[228:231], v[160:163], v[216:219]
	v_mfma_f32_16x16x32_bf16 v[44:47], v[168:171], v[164:167], v[44:47]
	v_mfma_f32_16x16x32_bf16 v[244:247], v[172:175], v[164:167], v[244:247]
	v_mfma_f32_16x16x32_bf16 v[220:223], v[176:179], v[164:167], v[220:223]
	v_mfma_f32_16x16x32_bf16 v[224:227], v[228:231], v[164:167], v[224:227]
	global_load_dwordx4 v[104:107], v[30:31], off offset:576
	global_load_dwordx4 v[108:111], v[32:33], off offset:576
	global_load_dwordx4 v[112:115], v[50:51], off offset:576
	global_load_dwordx4 v[116:119], v[54:55], off offset:576
	global_load_dwordx4 v[152:155], v[52:53], off offset:576
	global_load_dwordx4 v[156:159], v[56:57], off offset:576
	global_load_dwordx4 v[160:163], v[208:209], off offset:576
	global_load_dwordx4 v[164:167], v[210:211], off offset:576
	s_waitcnt vmcnt(16)
	v_mfma_f32_16x16x32_bf16 v[4:7], v[120:123], v[68:71], v[4:7]
	v_mfma_f32_16x16x32_bf16 v[8:11], v[124:127], v[68:71], v[8:11]
	v_mfma_f32_16x16x32_bf16 v[180:183], v[128:131], v[68:71], v[180:183]
	v_mfma_f32_16x16x32_bf16 v[184:187], v[132:135], v[68:71], v[184:187]
	v_mfma_f32_16x16x32_bf16 v[12:15], v[120:123], v[72:75], v[12:15]
	v_mfma_f32_16x16x32_bf16 v[16:19], v[124:127], v[72:75], v[16:19]
	v_mfma_f32_16x16x32_bf16 v[188:191], v[128:131], v[72:75], v[188:191]
	v_mfma_f32_16x16x32_bf16 v[192:195], v[132:135], v[72:75], v[192:195]
	v_mfma_f32_16x16x32_bf16 v[20:23], v[120:123], v[76:79], v[20:23]
	v_mfma_f32_16x16x32_bf16 v[24:27], v[124:127], v[76:79], v[24:27]
	v_mfma_f32_16x16x32_bf16 v[212:215], v[128:131], v[76:79], v[212:215]
	v_mfma_f32_16x16x32_bf16 v[216:219], v[132:135], v[76:79], v[216:219]
	v_mfma_f32_16x16x32_bf16 v[44:47], v[120:123], v[80:83], v[44:47]
	v_mfma_f32_16x16x32_bf16 v[244:247], v[124:127], v[80:83], v[244:247]
	v_mfma_f32_16x16x32_bf16 v[220:223], v[128:131], v[80:83], v[220:223]
	v_mfma_f32_16x16x32_bf16 v[224:227], v[132:135], v[80:83], v[224:227]
	global_load_dwordx4 v[168:171], v[30:31], off offset:640
	global_load_dwordx4 v[172:175], v[32:33], off offset:640
	global_load_dwordx4 v[176:179], v[50:51], off offset:640
	global_load_dwordx4 v[228:231], v[54:55], off offset:640
	global_load_dwordx4 v[68:71], v[52:53], off offset:640
	global_load_dwordx4 v[72:75], v[56:57], off offset:640
	global_load_dwordx4 v[76:79], v[208:209], off offset:640
	global_load_dwordx4 v[80:83], v[210:211], off offset:640
	s_waitcnt vmcnt(16)
	v_mfma_f32_16x16x32_bf16 v[4:7], v[136:139], v[84:87], v[4:7]
	v_mfma_f32_16x16x32_bf16 v[8:11], v[140:143], v[84:87], v[8:11]
	v_mfma_f32_16x16x32_bf16 v[180:183], v[144:147], v[84:87], v[180:183]
	v_mfma_f32_16x16x32_bf16 v[184:187], v[148:151], v[84:87], v[184:187]
	v_mfma_f32_16x16x32_bf16 v[12:15], v[136:139], v[88:91], v[12:15]
	v_mfma_f32_16x16x32_bf16 v[16:19], v[140:143], v[88:91], v[16:19]
	v_mfma_f32_16x16x32_bf16 v[188:191], v[144:147], v[88:91], v[188:191]
	v_mfma_f32_16x16x32_bf16 v[192:195], v[148:151], v[88:91], v[192:195]
	v_mfma_f32_16x16x32_bf16 v[20:23], v[136:139], v[92:95], v[20:23]
	v_mfma_f32_16x16x32_bf16 v[24:27], v[140:143], v[92:95], v[24:27]
	v_mfma_f32_16x16x32_bf16 v[212:215], v[144:147], v[92:95], v[212:215]
	v_mfma_f32_16x16x32_bf16 v[216:219], v[148:151], v[92:95], v[216:219]
	v_mfma_f32_16x16x32_bf16 v[44:47], v[136:139], v[100:103], v[44:47]
	v_mfma_f32_16x16x32_bf16 v[244:247], v[140:143], v[100:103], v[244:247]
	v_mfma_f32_16x16x32_bf16 v[220:223], v[144:147], v[100:103], v[220:223]
	v_mfma_f32_16x16x32_bf16 v[224:227], v[148:151], v[100:103], v[224:227]
	global_load_dwordx4 v[120:123], v[30:31], off offset:704
	global_load_dwordx4 v[124:127], v[32:33], off offset:704
	global_load_dwordx4 v[128:131], v[50:51], off offset:704
	global_load_dwordx4 v[132:135], v[54:55], off offset:704
	global_load_dwordx4 v[84:87], v[52:53], off offset:704
	global_load_dwordx4 v[88:91], v[56:57], off offset:704
	global_load_dwordx4 v[92:95], v[208:209], off offset:704
	global_load_dwordx4 v[100:103], v[210:211], off offset:704
	s_waitcnt vmcnt(16)
; template <int NS  > __device__ __forceinline__ f32x4 ctx_tile(Frame& F, const bf16* A, const bf16* Bt, int r0, int c0) {
;     ...
;     for (int s = 0; s < NS; ++s) {
;         bf16x8 af[4], bf[2];
; #pragma unroll
;         for (int rt = 0; rt < 4; ++rt) af[rt] = *(const bf16x8*)(ap + (size_t)(16 * rt) * K + 32 * s);
;         bf[0] = *(const bf16x8*)(bp + 32 * s); bf[1] = *(const bf16x8*)(bp + (size_t)16 * K + 32 * s);
; #pragma unroll
;         for (int rt = 0; rt < 4; ++rt) { acc[rt][0] = __builtin_amdgcn_mfma_f32_16x16x32_bf16(bf[0], af[rt], acc[rt][0], 0, 0, 0); acc[rt][1] = __builtin_amdgcn_mfma_f32_16x16x32_bf16(bf[1], af[rt], acc[rt][1], 0, 0, 0); }
;     }
	v_mfma_f32_16x16x32_bf16 v[4:7], v[152:155], v[104:107], v[4:7]
	v_mfma_f32_16x16x32_bf16 v[8:11], v[156:159], v[104:107], v[8:11]
	v_mfma_f32_16x16x32_bf16 v[180:183], v[160:163], v[104:107], v[180:183]
	v_mfma_f32_16x16x32_bf16 v[184:187], v[164:167], v[104:107], v[184:187]
	v_mfma_f32_16x16x32_bf16 v[12:15], v[152:155], v[108:111], v[12:15]
	v_mfma_f32_16x16x32_bf16 v[16:19], v[156:159], v[108:111], v[16:19]
	v_mfma_f32_16x16x32_bf16 v[188:191], v[160:163], v[108:111], v[188:191]
	v_mfma_f32_16x16x32_bf16 v[192:195], v[164:167], v[108:111], v[192:195]
	v_mfma_f32_16x16x32_bf16 v[20:23], v[152:155], v[112:115], v[20:23]
	v_mfma_f32_16x16x32_bf16 v[24:27], v[156:159], v[112:115], v[24:27]
	v_mfma_f32_16x16x32_bf16 v[212:215], v[160:163], v[112:115], v[212:215]
	v_mfma_f32_16x16x32_bf16 v[216:219], v[164:167], v[112:115], v[216:219]
	v_mfma_f32_16x16x32_bf16 v[44:47], v[152:155], v[116:119], v[44:47]
	v_mfma_f32_16x16x32_bf16 v[244:247], v[156:159], v[116:119], v[244:247]
	v_mfma_f32_16x16x32_bf16 v[220:223], v[160:163], v[116:119], v[220:223]
	v_mfma_f32_16x16x32_bf16 v[224:227], v[164:167], v[116:119], v[224:227]
	global_load_dwordx4 v[136:139], v[30:31], off offset:768
	global_load_dwordx4 v[140:143], v[32:33], off offset:768
	global_load_dwordx4 v[144:147], v[50:51], off offset:768
	global_load_dwordx4 v[148:151], v[54:55], off offset:768
	global_load_dwordx4 v[104:107], v[52:53], off offset:768
	global_load_dwordx4 v[108:111], v[56:57], off offset:768
	global_load_dwordx4 v[112:115], v[208:209], off offset:768
	global_load_dwordx4 v[116:119], v[210:211], off offset:768
	s_waitcnt vmcnt(16)
	v_mfma_f32_16x16x32_bf16 v[4:7], v[68:71], v[168:171], v[4:7]
	v_mfma_f32_16x16x32_bf16 v[8:11], v[72:75], v[168:171], v[8:11]
	v_mfma_f32_16x16x32_bf16 v[180:183], v[76:79], v[168:171], v[180:183]
	v_mfma_f32_16x16x32_bf16 v[184:187], v[80:83], v[168:171], v[184:187]
	v_mfma_f32_16x16x32_bf16 v[12:15], v[68:71], v[172:175], v[12:15]
	v_mfma_f32_16x16x32_bf16 v[16:19], v[72:75], v[172:175], v[16:19]
	v_mfma_f32_16x16x32_bf16 v[188:191], v[76:79], v[172:175], v[188:191]
	v_mfma_f32_16x16x32_bf16 v[192:195], v[80:83], v[172:175], v[192:195]
	v_mfma_f32_16x16x32_bf16 v[20:23], v[68:71], v[176:179], v[20:23]
	v_mfma_f32_16x16x32_bf16 v[24:27], v[72:75], v[176:179], v[24:27]
	v_mfma_f32_16x16x32_bf16 v[212:215], v[76:79], v[176:179], v[212:215]
	v_mfma_f32_16x16x32_bf16 v[216:219], v[80:83], v[176:179], v[216:219]
	v_mfma_f32_16x16x32_bf16 v[44:47], v[68:71], v[228:231], v[44:47]
	v_mfma_f32_16x16x32_bf16 v[244:247], v[72:75], v[228:231], v[244:247]
	v_mfma_f32_16x16x32_bf16 v[220:223], v[76:79], v[228:231], v[220:223]
	v_mfma_f32_16x16x32_bf16 v[224:227], v[80:83], v[228:231], v[224:227]
	global_load_dwordx4 v[152:155], v[30:31], off offset:832
	global_load_dwordx4 v[156:159], v[32:33], off offset:832
	global_load_dwordx4 v[160:163], v[50:51], off offset:832
	global_load_dwordx4 v[164:167], v[54:55], off offset:832
	global_load_dwordx4 v[168:171], v[52:53], off offset:832
	global_load_dwordx4 v[172:175], v[56:57], off offset:832
	global_load_dwordx4 v[176:179], v[208:209], off offset:832
	global_load_dwordx4 v[228:231], v[210:211], off offset:832
	s_waitcnt vmcnt(16)
	v_mfma_f32_16x16x32_bf16 v[4:7], v[84:87], v[120:123], v[4:7]
	v_mfma_f32_16x16x32_bf16 v[8:11], v[88:91], v[120:123], v[8:11]
	v_mfma_f32_16x16x32_bf16 v[180:183], v[92:95], v[120:123], v[180:183]
	v_mfma_f32_16x16x32_bf16 v[184:187], v[100:103], v[120:123], v[184:187]
	v_mfma_f32_16x16x32_bf16 v[12:15], v[84:87], v[124:127], v[12:15]
	v_mfma_f32_16x16x32_bf16 v[16:19], v[88:91], v[124:127], v[16:19]
	v_mfma_f32_16x16x32_bf16 v[188:191], v[92:95], v[124:127], v[188:191]
	v_mfma_f32_16x16x32_bf16 v[192:195], v[100:103], v[124:127], v[192:195]
	v_mfma_f32_16x16x32_bf16 v[20:23], v[84:87], v[128:131], v[20:23]
	v_mfma_f32_16x16x32_bf16 v[24:27], v[88:91], v[128:131], v[24:27]
	v_mfma_f32_16x16x32_bf16 v[212:215], v[92:95], v[128:131], v[212:215]
	v_mfma_f32_16x16x32_bf16 v[216:219], v[100:103], v[128:131], v[216:219]
	v_mfma_f32_16x16x32_bf16 v[44:47], v[84:87], v[132:135], v[44:47]
	v_mfma_f32_16x16x32_bf16 v[244:247], v[88:91], v[132:135], v[244:247]
	v_mfma_f32_16x16x32_bf16 v[220:223], v[92:95], v[132:135], v[220:223]
	v_mfma_f32_16x16x32_bf16 v[224:227], v[100:103], v[132:135], v[224:227]
	s_waitcnt vmcnt(8)
	v_mfma_f32_16x16x32_bf16 v[4:7], v[104:107], v[136:139], v[4:7]
	v_mfma_f32_16x16x32_bf16 v[8:11], v[108:111], v[136:139], v[8:11]
	v_mfma_f32_16x16x32_bf16 v[180:183], v[112:115], v[136:139], v[180:183]
	v_mfma_f32_16x16x32_bf16 v[184:187], v[116:119], v[136:139], v[184:187]
	v_mfma_f32_16x16x32_bf16 v[12:15], v[104:107], v[140:143], v[12:15]
	v_mfma_f32_16x16x32_bf16 v[16:19], v[108:111], v[140:143], v[16:19]
	v_mfma_f32_16x16x32_bf16 v[188:191], v[112:115], v[140:143], v[188:191]
	v_mfma_f32_16x16x32_bf16 v[192:195], v[116:119], v[140:143], v[192:195]
	v_mfma_f32_16x16x32_bf16 v[20:23], v[104:107], v[144:147], v[20:23]
	v_mfma_f32_16x16x32_bf16 v[24:27], v[108:111], v[144:147], v[24:27]
	v_mfma_f32_16x16x32_bf16 v[212:215], v[112:115], v[144:147], v[212:215]
	v_mfma_f32_16x16x32_bf16 v[216:219], v[116:119], v[144:147], v[216:219]
	v_mfma_f32_16x16x32_bf16 v[44:47], v[104:107], v[148:151], v[44:47]
	v_mfma_f32_16x16x32_bf16 v[244:247], v[108:111], v[148:151], v[244:247]
	v_mfma_f32_16x16x32_bf16 v[220:223], v[112:115], v[148:151], v[220:223]
	v_mfma_f32_16x16x32_bf16 v[224:227], v[116:119], v[148:151], v[224:227]
	s_waitcnt vmcnt(0)
	v_mfma_f32_16x16x32_bf16 v[4:7], v[168:171], v[152:155], v[4:7]
	v_mfma_f32_16x16x32_bf16 v[8:11], v[172:175], v[152:155], v[8:11]
	v_mfma_f32_16x16x32_bf16 v[180:183], v[176:179], v[152:155], v[180:183]
	v_mfma_f32_16x16x32_bf16 v[184:187], v[228:231], v[152:155], v[184:187]
	v_mfma_f32_16x16x32_bf16 v[12:15], v[168:171], v[156:159], v[12:15]
	v_mfma_f32_16x16x32_bf16 v[16:19], v[172:175], v[156:159], v[16:19]
	v_mfma_f32_16x16x32_bf16 v[188:191], v[176:179], v[156:159], v[188:191]
	v_mfma_f32_16x16x32_bf16 v[192:195], v[228:231], v[156:159], v[192:195]
	v_mfma_f32_16x16x32_bf16 v[20:23], v[168:171], v[160:163], v[20:23]
	v_mfma_f32_16x16x32_bf16 v[24:27], v[172:175], v[160:163], v[24:27]
	v_mfma_f32_16x16x32_bf16 v[212:215], v[176:179], v[160:163], v[212:215]
	v_mfma_f32_16x16x32_bf16 v[216:219], v[228:231], v[160:163], v[216:219]
	v_mfma_f32_16x16x32_bf16 v[44:47], v[168:171], v[164:167], v[44:47]
	v_mfma_f32_16x16x32_bf16 v[244:247], v[172:175], v[164:167], v[244:247]
	v_mfma_f32_16x16x32_bf16 v[220:223], v[176:179], v[164:167], v[220:223]
	v_mfma_f32_16x16x32_bf16 v[224:227], v[228:231], v[164:167], v[224:227]
	v_or_b32_e32 v61, s15, v1
	s_add_i32 s29, s29, s28
	s_add_i32 s11, s11, s12
	s_add_i32 s13, s13, s14
	s_cmp_ge_i32 s29, s10
	v_mov_b32_e32 v67, v98
	s_barrier
; #define LAS __attribute__((address_space(3)))
; __device__ __forceinline__ unsigned pk2(float lo, float hi) { f32x2 v = {lo, hi}; return __builtin_bit_cast(unsigned, __builtin_convertvector(v, bf2_t)); }
; template <int NS  > __device__ __forceinline__ f32x4 ctx_tile(Frame& F, const bf16* A, const bf16* Bt, int r0, int c0) {
;     ...
;     LAS f32x4* red = (LAS f32x4*)F.lds;
;     __syncthreads();
; #pragma unroll
;     for (int rt = 0; rt < 4; ++rt) { red[(w * 8 + 2 * rt) * 64 + lane] = acc[rt][0]; red[(w * 8 + 2 * rt + 1) * 64 + lane] = acc[rt][1]; }
;     __syncthreads();
;     const int tt = F.tid >> 6;
;     f32x4 v = red[tt * 64 + lane];
; #pragma unroll
;     for (int ww = 1; ww < 8; ++ww) v = v + red[(ww * 8 + tt) * 64 + lane];
;     return v;
; }
; __global__ void __launch_bounds__(NWAVES * 64, 2) mk_fwd(Args args) {
;     ...
;                     const int tt = F.tid >> 6; const size_t row = (size_t)(r0 + 16 * (tt >> 1) + (F.lane & 15)); const int col = c0 + 16 * (tt & 1) + 4 * (F.lane >> 4);
;                     u32x2 o2; o2.x = pk2(s[0], s[1]); o2.y = pk2(s[2], s[3]);
;                     *(u32x2*)((bf16*)(ws + WS_FS) + row * D + col) = o2;
	v_lshlrev_b32_e32 v66, 1, v61
	v_add_u32_e32 v42, s16, v65
	v_ashrrev_i32_e32 v43, 31, v42
	v_lshlrev_b64 v[42:43], 11, v[42:43]
	v_lshl_add_u64 v[38:39], s[0:1], 0, v[42:43]
	v_lshl_add_u64 v[38:39], v[38:39], 0, v[66:67]
	s_nop 7
	ds_write_b128 v63, v[180:183]
	ds_write_b128 v63, v[184:187] offset:1024
	ds_write_b128 v63, v[188:191] offset:2048
	ds_write_b128 v63, v[192:195] offset:3072
	ds_write_b128 v63, v[212:215] offset:4096
	ds_write_b128 v63, v[216:219] offset:5120
	ds_write_b128 v63, v[220:223] offset:6144
	ds_write_b128 v63, v[224:227] offset:7168
	s_waitcnt lgkmcnt(0)
	s_barrier
	ds_read_b128 v[100:103], v64
	ds_read_b128 v[104:107], v64 offset:8192
	ds_read_b128 v[108:111], v64 offset:16384
	ds_read_b128 v[112:115], v64 offset:24576
	ds_read_b128 v[116:119], v64 offset:32768
	ds_read_b128 v[120:123], v64 offset:40960
	ds_read_b128 v[124:127], v64 offset:49152
	ds_read_b128 v[128:131], v64 offset:57344
	s_waitcnt lgkmcnt(6)
	v_pk_add_f32 v[102:103], v[102:103], v[106:107]
	v_pk_add_f32 v[100:101], v[100:101], v[104:105]
	s_waitcnt lgkmcnt(5)
	v_pk_add_f32 v[102:103], v[102:103], v[110:111]
	v_pk_add_f32 v[100:101], v[100:101], v[108:109]
	s_waitcnt lgkmcnt(4)
	v_pk_add_f32 v[102:103], v[102:103], v[114:115]
	v_pk_add_f32 v[100:101], v[100:101], v[112:113]
	s_waitcnt lgkmcnt(3)
	v_pk_add_f32 v[102:103], v[102:103], v[118:119]
	v_pk_add_f32 v[100:101], v[100:101], v[116:117]
	s_waitcnt lgkmcnt(2)
	v_pk_add_f32 v[102:103], v[102:103], v[122:123]
	v_pk_add_f32 v[100:101], v[100:101], v[120:121]
	s_waitcnt lgkmcnt(1)
	v_pk_add_f32 v[102:103], v[102:103], v[126:127]
	v_pk_add_f32 v[100:101], v[100:101], v[124:125]
	s_waitcnt lgkmcnt(0)
	v_pk_add_f32 v[102:103], v[102:103], v[130:131]
	v_pk_add_f32 v[100:101], v[100:101], v[128:129]
	s_nop 0
	v_cvt_pk_bf16_f32 v100, v100, v101
	v_cvt_pk_bf16_f32 v101, v102, v103
	global_store_dwordx2 v[38:39], v[100:101], off offset:64
	s_barrier
	ds_write_b128 v63, v[4:7]
	ds_write_b128 v63, v[8:11] offset:1024
	ds_write_b128 v63, v[12:15] offset:2048
	ds_write_b128 v63, v[16:19] offset:3072
	ds_write_b128 v63, v[20:23] offset:4096
	ds_write_b128 v63, v[24:27] offset:5120
	ds_write_b128 v63, v[44:47] offset:6144
	ds_write_b128 v63, v[244:247] offset:7168
	s_waitcnt lgkmcnt(0)
	s_barrier
	ds_read_b128 v[2:5], v64
	ds_read_b128 v[6:9], v64 offset:8192
	ds_read_b128 v[10:13], v64 offset:16384
	ds_read_b128 v[14:17], v64 offset:24576
	ds_read_b128 v[18:21], v64 offset:32768
	ds_read_b128 v[22:25], v64 offset:40960
	ds_read_b128 v[26:29], v64 offset:49152
	ds_read_b128 v[30:33], v64 offset:57344
	s_waitcnt lgkmcnt(6)
	v_pk_add_f32 v[4:5], v[4:5], v[8:9]
	v_pk_add_f32 v[2:3], v[2:3], v[6:7]
	s_waitcnt lgkmcnt(5)
	v_pk_add_f32 v[4:5], v[4:5], v[12:13]
	v_pk_add_f32 v[2:3], v[2:3], v[10:11]
	s_waitcnt lgkmcnt(4)
	v_pk_add_f32 v[4:5], v[4:5], v[16:17]
	v_pk_add_f32 v[2:3], v[2:3], v[14:15]
	s_waitcnt lgkmcnt(3)
	v_pk_add_f32 v[4:5], v[4:5], v[20:21]
	v_pk_add_f32 v[2:3], v[2:3], v[18:19]
	s_waitcnt lgkmcnt(2)
	v_pk_add_f32 v[4:5], v[4:5], v[24:25]
	v_pk_add_f32 v[2:3], v[2:3], v[22:23]
	s_waitcnt lgkmcnt(1)
	v_pk_add_f32 v[4:5], v[4:5], v[28:29]
	v_pk_add_f32 v[2:3], v[2:3], v[26:27]
	s_waitcnt lgkmcnt(0)
	v_pk_add_f32 v[4:5], v[4:5], v[32:33]
	v_pk_add_f32 v[2:3], v[2:3], v[30:31]
	s_nop 0
	v_cvt_pk_bf16_f32 v2, v2, v3
	v_cvt_pk_bf16_f32 v3, v4, v5
	global_store_dwordx2 v[38:39], v[2:3], off
	s_cbranch_scc0 .LBB13_1582
